# fp8 GEMM phase tails (P8, P11, P15): workgroups with one more GEMM unit now also convert a few weight tiles (one unit ~ 6 tiles) instead of skipping the background conversion
# speedup vs baseline: 1.0097x; 1.0022x over previous
; DI void cvt_group(const Params& p, LAS unsigned char* lds, int group, int t_lo, int t_hi, int r, int I) {
;     ...
;     if (tid == 0) {
;         int t0 = 0, nj = 0;
;         if (group == 0) {
;             set_job(J, 0, p.in[11], (bf16_t*)(ws + WS_W0IN), DM, L0IN, DM, 0, 1, 0, 0, t0);
;             set_job(J, 1, p.in[13], (bf16_t*)(ws + WS_WUQ), 512, 1536, 512, 0, 1, 0, 0, t0);
;             set_job(J, 2, p.in[15], (bf16_t*)(ws + WS_WUKV), 256, 2048, 256, 0, 1, 0, 0, t0);
;             set_job(J, 3, p.in[23], (bf16_t*)(ws + WS_W0OUT), DM, DM, DM, 0, 1, 0, 0, t0);
;             set_job(J, 4, p.in[31], (bf16_t*)(ws + WS_W1IN), DM, L1IN, DM, 1, 1, 0, 0, t0); if (FP8_IN1) J[4].f8scale = 64.f;
;             set_job(J, 5, p.in[34], (bf16_t*)(ws + WS_W1OUT), DM, DM, DM, 0, 1, 0, 0, t0); if (FP8_OUT1) J[5].f8scale = 64.f;
;             set_job(J, 6, p.in[18], (bf16_t*)(ws + WS_GW), 128, 128, 128, 0, 16, 128 * 128, 128 * 128, t0);
;             set_job(J, 7, p.in[20], (bf16_t*)(ws + WS_GW + (size_t)16 * 128 * 128 * 2), 128, 128, 128, 0, 16, 128 * 128, 128 * 128, t0);
;             nj = 8;
;         } else if (group == 1) {
;             set_job(J, 0, p.in[24], (bf16_t*)(ws + WS_EG), DM, EFF, DM, 0, NEXP, (size_t)DM * EFF, (size_t)EFF * DM, t0);
;             set_job(J, 1, p.in[25], (bf16_t*)(ws + WS_EU), DM, EFF, DM, 0, NEXP, (size_t)DM * EFF, (size_t)EFF * DM, t0);
;             set_job(J, 2, p.in[26], (bf16_t*)(ws + WS_ED), EFF, DM, EFF, 0, NEXP, (size_t)DM * EFF, (size_t)EFF * DM, t0);
;             if (FP8_L0) { J[0].f8scale = 64.f; J[1].f8scale = 64.f; J[2].f8scale = 32.f; }
;             nj = 3;
;         } else {
;             set_job(J, 0, p.in[35], (bf16_t*)(ws + WS_EG + EXPW), DM, EFF, DM, 0, NEXP, (size_t)DM * EFF, (size_t)EFF * DM, t0); J[0].f8scale = 64.f;
;             set_job(J, 1, p.in[36], (bf16_t*)(ws + WS_EU + EXPW), DM, EFF, DM, 0, NEXP, (size_t)DM * EFF, (size_t)EFF * DM, t0); J[1].f8scale = 64.f;
;             set_job(J, 2, p.in[37], (bf16_t*)(ws + WS_ED + EXPW), EFF, DM, EFF, 0, NEXP, (size_t)DM * EFF, (size_t)EFF * DM, t0); J[2].f8scale = 32.f;
;             nj = 3;
;         }
;         J[nj].tile0 = t0; J[15].tile0 = nj;
;     }
;     __syncthreads();
;     const int nj = J[15].tile0, total = J[nj].tile0;
;     const int hi = min(t_hi, total);
;     const int row = tid >> 6, c4 = (tid & 63) * 4;
;     for (int gt = t_lo + r; gt < hi; gt += I) {
.LBB0_915:
	s_add_u32 s18, s50, 0x710e000
	s_addc_u32 s19, s51, 0
	s_add_u32 s16, s50, 0xf10e000
	s_addc_u32 s17, s51, 0
	s_add_u32 s14, s50, 0x1710e000
	s_addc_u32 s15, s51, 0
	s_abs_i32 s0, s23
	v_cvt_f32_u32_e32 v3, s0
	s_sub_i32 s5, 0, s0
	s_abs_i32 s4, s9
	s_ashr_i32 s1, s9, 31
	v_rcp_iflag_f32_e32 v3, v3
	v_and_b32_e32 v11, 0xff, v0
	v_lshlrev_b32_e32 v4, 1, v0
	v_mul_u32_u24_e32 v2, 0x410, v198
	v_mul_f32_e32 v3, 0x4f7ffffe, v3
	v_cvt_u32_f32_e32 v3, v3
	v_and_b32_e32 v10, 0xfc, v199
	v_and_b32_e32 v4, 32, v4
	v_lshl_add_u32 v16, v11, 2, 0
	v_readfirstlane_b32 s6, v3
	s_mul_i32 s5, s5, s6
	s_mul_hi_u32 s5, s6, s5
	s_add_i32 s6, s6, s5
	s_mul_hi_u32 s5, s4, s6
	s_mul_i32 s5, s5, s0
	s_sub_i32 s4, s4, s5
	s_sub_i32 s5, s4, s0
	s_cmp_ge_u32 s4, s0
	s_cselect_b32 s4, s5, s4
	s_sub_i32 s5, s4, s0
	s_cmp_ge_u32 s4, s0
	s_cselect_b32 s0, s5, s4
	s_xor_b32 s0, s0, s1
	s_sub_i32 s4, s0, s1
	v_mul_u32_u24_e32 v14, 0x410, v222
	v_mul_u32_u24_e32 v13, 0x410, v223
	v_cmp_eq_u32_e64 s[2:3], 0, v0
	v_mov_b32_e32 v199, 0
	v_lshl_add_u32 v15, v10, 2, 0
	v_and_or_b32 v1, v1, 16, v4
	s_cmp_lg_u32 s4, 0
	v_add_u32_e32 v12, v16, v2
	s_cbranch_scc0 .LBB0_938
	s_waitcnt vmcnt(0)
	s_barrier
	s_and_saveexec_b64 s[0:1], s[2:3]
	s_cbranch_execz .LBB0_919
	s_movk_i32 s8, 0x800
	s_mov_b32 s11, 0
	s_add_i32 s5, 0, 0x12000
	s_mov_b32 s10, s8
	v_mov_b32_e32 v2, s42
	v_mov_b32_e32 v3, s43
	v_mov_b32_e32 v4, s18
	v_mov_b32_e32 v5, s19
	v_mov_b32_e32 v6, s5
	s_movk_i32 s9, 0x200
	s_add_i32 s5, 0, 0x12010
	v_mov_b64_e32 v[24:25], s[10:11]
	ds_write_b128 v6, v[2:5]
	v_mov_b32_e32 v2, s5
	v_mov_b64_e32 v[22:23], s[8:9]
	s_add_i32 s5, 0, 0x12020
	s_mov_b32 s6, 0x100000
	ds_write_b128 v2, v[22:25]
	v_mov_b32_e32 v8, 64
	v_mov_b32_e32 v9, 0
	v_mov_b32_e32 v2, s5
	s_add_i32 s5, 0, 0x12028
	s_mov_b32 s7, s11
	s_mov_b32 s10, s6
	ds_write_b64 v2, v[8:9]
	v_mov_b32_e32 v2, s5
	v_mov_b64_e32 v[18:19], s[6:7]
	v_mov_b64_e32 v[20:21], s[10:11]
	s_add_i32 s5, 0, 0x12040
	ds_write2_b64 v2, v[18:19], v[20:21] offset1:1
	v_mov_b32_e32 v2, s44
	v_mov_b32_e32 v3, s45
	v_mov_b32_e32 v4, s16
	v_mov_b32_e32 v5, s17
	v_mov_b32_e32 v6, s5
	s_add_i32 s5, 0, 0x12050
	ds_write_b128 v6, v[2:5]
	v_mov_b32_e32 v2, s5
	s_add_i32 s5, 0, 0x12060
	ds_write_b128 v2, v[22:25]
	v_mov_b32_e32 v3, 0x800
	v_mov_b32_e32 v2, v8
	v_mov_b32_e32 v4, s5
	s_add_i32 s5, 0, 0x12068
	ds_write_b64 v4, v[2:3]
	v_mov_b32_e32 v2, s5
	s_add_i32 s5, 0, 0x12080
	ds_write2_b64 v2, v[18:19], v[20:21] offset1:1
	v_mov_b32_e32 v4, s46
	v_mov_b32_e32 v5, s47
	v_mov_b32_e32 v6, s14
	v_mov_b32_e32 v7, s15
	v_mov_b32_e32 v2, s5
	ds_write_b128 v2, v[4:7]
	v_mov_b32_e32 v2, 0x200
	s_add_i32 s5, 0, 0x12090
	v_mov_b32_e32 v4, v2
	v_mov_b32_e32 v5, v9
	v_mov_b32_e32 v6, s5
	s_add_i32 s5, 0, 0x120a0
	ds_write_b128 v6, v[2:5]
	v_mov_b32_e32 v9, 0x1000
	v_mov_b32_e32 v2, s5
	s_add_i32 s5, 0, 0x120a8
	ds_write_b64 v2, v[8:9]
	v_mov_b32_e32 v2, s5
	s_add_i32 s5, 0, 0x12038
	ds_write2_b64 v2, v[18:19], v[20:21] offset1:1
	v_mov_b32_e32 v2, 0x42800000
	v_mov_b32_e32 v3, s5
	s_add_i32 s5, 0, 0x12078
	ds_write_b32 v3, v2
	v_mov_b32_e32 v3, s5
	s_add_i32 s5, 0, 0x120b8
	ds_write_b32 v3, v2
	v_mov_b32_e32 v2, 0x42000000
	v_mov_b32_e32 v3, s5
	s_add_i32 s5, 0, 0x120e4
	ds_write_b32 v3, v2
	v_mov_b32_e32 v2, 0x1800
	v_mov_b32_e32 v3, s5
	s_add_i32 s5, 0, 0x123e4
	ds_write_b32 v3, v2
	v_mov_b32_e32 v2, 3
	v_mov_b32_e32 v3, s5
	ds_write_b32 v3, v2
.LBB0_919:
	s_or_b64 exec, exec, s[0:1]
	s_add_i32 s0, 0, 0x123e4
	v_mov_b32_e32 v2, s0
	s_waitcnt lgkmcnt(0)
	s_barrier
	ds_read_b32 v2, v2
	s_sub_i32 s31, s23, s4
	s_mul_i32 s0, s31, 6
	s_sub_i32 s0, 0x960, s0
	s_max_i32 s0, s0, 0
	s_lshr_b32 s0, s0, 8
	s_cmpk_lg_i32 s23, 0x100
	s_cselect_b32 s0, 0, s0
	s_mul_i32 s0, s0, s4
	s_sub_i32 s1, 0x960, s0
	s_sub_i32 s27, s22, s4
	s_nop 0
	s_add_i32 s0, s1, s22
	s_cmp_lt_i32 s22, s4
	s_cselect_b32 s27, s0, s27
	s_cselect_b32 s31, s4, s31
	s_cselect_b32 s1, 0x960, s1
	s_waitcnt lgkmcnt(0)
	v_lshlrev_b32_e32 v3, 6, v2
	v_add_u32_e32 v3, 0, v3
	v_add_u32_e32 v3, 0x12024, v3
	ds_read_b32 v3, v3
	v_readfirstlane_b32 s30, v2
	s_waitcnt lgkmcnt(0)
	v_min_i32_e32 v17, s1, v3
	v_cmp_ge_i32_e32 vcc, s27, v17
	s_cbranch_vccnz .LBB0_937
	s_cmp_gt_i32 s30, 1
	s_cselect_b64 s[0:1], -1, 0
	s_add_i32 s4, s30, -1
	s_cmp_lg_u32 s30, 2
	v_cndmask_b32_e64 v2, 0, 1, s[0:1]
	s_cselect_b64 s[0:1], -1, 0
	s_and_b32 s34, s4, -2
	s_or_b32 s35, s4, 1
	s_cmp_lg_u32 s4, s34
	v_cndmask_b32_e64 v4, 0, 1, s[0:1]
	s_cselect_b64 s[8:9], -1, 0
	v_cmp_ne_u32_e64 s[4:5], 1, v2
	s_add_i32 s40, 0, 0x120a4
	s_brev_b32 s41, 1
	v_lshlrev_b32_e32 v2, 2, v10
	v_mov_b32_e32 v3, 0
	v_add_u32_e32 v18, v15, v14
	s_movk_i32 s54, 0x4ff
	s_movk_i32 s55, 0xffcf
	s_mov_b32 s58, 0xc3e00000
	v_cmp_ne_u32_e64 s[6:7], 1, v4
	v_mov_b32_e32 v19, 0x43e00000
	s_branch .LBB0_923

; DI void cvt_group(const Params& p, LAS unsigned char* lds, int group, int t_lo, int t_hi, int r, int I) {
;     ...
;     if (tid == 0) {
;         int t0 = 0, nj = 0;
;         if (group == 0) {
;             set_job(J, 0, p.in[11], (bf16_t*)(ws + WS_W0IN), DM, L0IN, DM, 0, 1, 0, 0, t0);
;             set_job(J, 1, p.in[13], (bf16_t*)(ws + WS_WUQ), 512, 1536, 512, 0, 1, 0, 0, t0);
;             set_job(J, 2, p.in[15], (bf16_t*)(ws + WS_WUKV), 256, 2048, 256, 0, 1, 0, 0, t0);
;             set_job(J, 3, p.in[23], (bf16_t*)(ws + WS_W0OUT), DM, DM, DM, 0, 1, 0, 0, t0);
;             set_job(J, 4, p.in[31], (bf16_t*)(ws + WS_W1IN), DM, L1IN, DM, 1, 1, 0, 0, t0); if (FP8_IN1) J[4].f8scale = 64.f;
;             set_job(J, 5, p.in[34], (bf16_t*)(ws + WS_W1OUT), DM, DM, DM, 0, 1, 0, 0, t0); if (FP8_OUT1) J[5].f8scale = 64.f;
;             set_job(J, 6, p.in[18], (bf16_t*)(ws + WS_GW), 128, 128, 128, 0, 16, 128 * 128, 128 * 128, t0);
;             set_job(J, 7, p.in[20], (bf16_t*)(ws + WS_GW + (size_t)16 * 128 * 128 * 2), 128, 128, 128, 0, 16, 128 * 128, 128 * 128, t0);
;             nj = 8;
;         } else if (group == 1) {
;             set_job(J, 0, p.in[24], (bf16_t*)(ws + WS_EG), DM, EFF, DM, 0, NEXP, (size_t)DM * EFF, (size_t)EFF * DM, t0);
;             set_job(J, 1, p.in[25], (bf16_t*)(ws + WS_EU), DM, EFF, DM, 0, NEXP, (size_t)DM * EFF, (size_t)EFF * DM, t0);
;             set_job(J, 2, p.in[26], (bf16_t*)(ws + WS_ED), EFF, DM, EFF, 0, NEXP, (size_t)DM * EFF, (size_t)EFF * DM, t0);
;             if (FP8_L0) { J[0].f8scale = 64.f; J[1].f8scale = 64.f; J[2].f8scale = 32.f; }
;             nj = 3;
;         } else {
;             set_job(J, 0, p.in[35], (bf16_t*)(ws + WS_EG + EXPW), DM, EFF, DM, 0, NEXP, (size_t)DM * EFF, (size_t)EFF * DM, t0); J[0].f8scale = 64.f;
;             set_job(J, 1, p.in[36], (bf16_t*)(ws + WS_EU + EXPW), DM, EFF, DM, 0, NEXP, (size_t)DM * EFF, (size_t)EFF * DM, t0); J[1].f8scale = 64.f;
;             set_job(J, 2, p.in[37], (bf16_t*)(ws + WS_ED + EXPW), EFF, DM, EFF, 0, NEXP, (size_t)DM * EFF, (size_t)EFF * DM, t0); J[2].f8scale = 32.f;
;             nj = 3;
;         }
;         J[nj].tile0 = t0; J[15].tile0 = nj;
;     }
;     __syncthreads();
;     const int nj = J[15].tile0, total = J[nj].tile0;
;     const int hi = min(t_hi, total);
;     const int row = tid >> 6, c4 = (tid & 63) * 4;
;     for (int gt = t_lo + r; gt < hi; gt += I) {
.LBB0_1243:
	s_add_u32 s18, s50, 0x710e000
	s_addc_u32 s19, s51, 0
	s_add_u32 s16, s50, 0xf10e000
	s_addc_u32 s17, s51, 0
	s_add_u32 s14, s50, 0x1710e000
	s_addc_u32 s15, s51, 0
	s_abs_i32 s0, s23
	v_cvt_f32_u32_e32 v4, s0
	v_lshlrev_b32_e32 v2, 1, v0
	v_and_b32_e32 v13, 0xff, v0
	v_and_b32_e32 v2, 32, v2
	v_rcp_iflag_f32_e32 v4, v4
	v_lshrrev_b32_e32 v5, 1, v0
	v_and_or_b32 v14, v5, 16, v2
	v_and_b32_e32 v2, 32, v1
	v_mul_f32_e32 v4, 0x4f7ffffe, v4
	v_cvt_u32_f32_e32 v4, v4
	v_lshl_add_u32 v17, v13, 2, 0
	s_movk_i32 s1, 0x410
	v_mad_u32_u24 v15, v2, s1, v17
	s_sub_i32 s1, 0, s0
	v_readfirstlane_b32 s4, v4
	s_mul_i32 s1, s1, s4
	s_mul_hi_u32 s1, s4, s1
	s_add_i32 s4, s4, s1
	s_mul_hi_u32 s1, s4, 0x268
	s_mul_i32 s1, s1, s0
	s_sub_i32 s1, 0x268, s1
	s_sub_i32 s4, s1, s0
	s_cmp_ge_u32 s1, s0
	s_cselect_b32 s1, s4, s1
	s_sub_i32 s4, s1, s0
	s_cmp_ge_u32 s1, s0
	v_and_b32_e32 v12, 0xfc, v184
	v_or_b32_e32 v1, 31, v1
	s_cselect_b32 s4, s4, s1
	v_cmp_eq_u32_e64 s[2:3], 0, v0
	v_mov_b32_e32 v3, 0
	v_lshl_add_u32 v16, v12, 2, 0
	v_mul_u32_u24_e32 v18, 0x410, v222
	s_cmp_lg_u32 s4, 0
	v_mul_u32_u24_e32 v1, 0x410, v1
	s_cbranch_scc0 .LBB0_1266
	s_waitcnt vmcnt(0) lgkmcnt(0)
	s_barrier
	s_and_saveexec_b64 s[0:1], s[2:3]
	s_cbranch_execz .LBB0_1247
	s_movk_i32 s8, 0x800
	s_mov_b32 s11, 0
	s_add_i32 s5, 0, 0x12000
	s_mov_b32 s10, s8
	v_mov_b32_e32 v4, s42
	v_mov_b32_e32 v5, s43
	v_mov_b32_e32 v6, s18
	v_mov_b32_e32 v7, s19
	v_mov_b32_e32 v8, s5
	s_movk_i32 s9, 0x200
	s_add_i32 s5, 0, 0x12010
	v_mov_b64_e32 v[26:27], s[10:11]
	ds_write_b128 v8, v[4:7]
	v_mov_b32_e32 v4, s5
	v_mov_b64_e32 v[24:25], s[8:9]
	s_add_i32 s5, 0, 0x12020
	s_mov_b32 s6, 0x100000
	ds_write_b128 v4, v[24:27]
	v_mov_b32_e32 v10, 64
	v_mov_b32_e32 v11, 0
	v_mov_b32_e32 v4, s5
	s_add_i32 s5, 0, 0x12028
	s_mov_b32 s7, s11
	s_mov_b32 s10, s6
	ds_write_b64 v4, v[10:11]
	v_mov_b32_e32 v4, s5
	v_mov_b64_e32 v[20:21], s[6:7]
	v_mov_b64_e32 v[22:23], s[10:11]
	s_add_i32 s5, 0, 0x12040
	ds_write2_b64 v4, v[20:21], v[22:23] offset1:1
	v_mov_b32_e32 v4, s44
	v_mov_b32_e32 v5, s45
	v_mov_b32_e32 v6, s16
	v_mov_b32_e32 v7, s17
	v_mov_b32_e32 v8, s5
	s_add_i32 s5, 0, 0x12050
	ds_write_b128 v8, v[4:7]
	v_mov_b32_e32 v4, s5
	s_add_i32 s5, 0, 0x12060
	ds_write_b128 v4, v[24:27]
	v_mov_b32_e32 v5, 0x800
	v_mov_b32_e32 v4, v10
	v_mov_b32_e32 v6, s5
	s_add_i32 s5, 0, 0x12068
	ds_write_b64 v6, v[4:5]
	v_mov_b32_e32 v4, s5
	s_add_i32 s5, 0, 0x12080
	ds_write2_b64 v4, v[20:21], v[22:23] offset1:1
	v_mov_b32_e32 v6, s46
	v_mov_b32_e32 v7, s47
	v_mov_b32_e32 v8, s14
	v_mov_b32_e32 v9, s15
	v_mov_b32_e32 v4, s5
	ds_write_b128 v4, v[6:9]
	v_mov_b32_e32 v4, 0x200
	s_add_i32 s5, 0, 0x12090
	v_mov_b32_e32 v6, v4
	v_mov_b32_e32 v7, v11
	v_mov_b32_e32 v8, s5
	s_add_i32 s5, 0, 0x120a0
	ds_write_b128 v8, v[4:7]
	v_mov_b32_e32 v11, 0x1000
	v_mov_b32_e32 v4, s5
	s_add_i32 s5, 0, 0x120a8
	ds_write_b64 v4, v[10:11]
	v_mov_b32_e32 v4, s5
	s_add_i32 s5, 0, 0x12038
	ds_write2_b64 v4, v[20:21], v[22:23] offset1:1
	v_mov_b32_e32 v4, 0x42800000
	v_mov_b32_e32 v5, s5
	s_add_i32 s5, 0, 0x12078
	ds_write_b32 v5, v4
	v_mov_b32_e32 v5, s5
	s_add_i32 s5, 0, 0x120b8
	ds_write_b32 v5, v4
	v_mov_b32_e32 v4, 0x42000000
	v_mov_b32_e32 v5, s5
	s_add_i32 s5, 0, 0x120e4
	ds_write_b32 v5, v4
	v_mov_b32_e32 v4, 0x1800
	v_mov_b32_e32 v5, s5
	s_add_i32 s5, 0, 0x123e4
	ds_write_b32 v5, v4
	v_mov_b32_e32 v4, 3
	v_mov_b32_e32 v5, s5
	ds_write_b32 v5, v4
.LBB0_1247:
	s_or_b64 exec, exec, s[0:1]
	s_add_i32 s0, 0, 0x123e4
	v_mov_b32_e32 v4, s0
	s_waitcnt lgkmcnt(0)
	s_barrier
	ds_read_b32 v4, v4
	s_sub_i32 s34, s23, s4
	s_mul_i32 s0, s34, 6
	s_sub_i32 s0, 0x6a0, s0
	s_max_i32 s0, s0, 0
	s_lshr_b32 s0, s0, 8
	s_cmpk_lg_i32 s23, 0x100
	s_cselect_b32 s0, 0, s0
	s_mul_i32 s0, s0, s4
	s_sub_i32 s27, 0x1000, s0
	s_sub_i32 s30, s22, s4
	s_add_i32 s30, s30, 0x960
	s_add_i32 s0, s27, s22
	s_cmp_lt_i32 s22, s4
	s_cselect_b32 s30, s0, s30
	s_cselect_b32 s34, s4, s34
	s_cselect_b32 s27, 0x1000, s27
	s_waitcnt lgkmcnt(0)
	v_lshlrev_b32_e32 v5, 6, v4
	v_add_u32_e32 v5, 0, v5
	v_add_u32_e32 v5, 0x12024, v5
	ds_read_b32 v5, v5
	v_readfirstlane_b32 s31, v4
	s_waitcnt lgkmcnt(0)
	v_readfirstlane_b32 s1, v5
	s_min_i32 s27, s1, s27
	s_cmp_ge_i32 s30, s27
	s_cbranch_scc1 .LBB0_1265
	s_cmp_gt_i32 s31, 1
	s_cselect_b64 s[0:1], -1, 0
	s_add_i32 s4, s31, -1
	s_cmp_lg_u32 s31, 2
	v_cndmask_b32_e64 v4, 0, 1, s[0:1]
	s_cselect_b64 s[0:1], -1, 0
	s_and_b32 s35, s4, -2
	s_or_b32 s40, s4, 1
	s_cmp_lg_u32 s4, s35
	v_cndmask_b32_e64 v6, 0, 1, s[0:1]
	s_cselect_b64 s[8:9], -1, 0
	v_cmp_ne_u32_e64 s[4:5], 1, v4
	s_add_i32 s41, 0, 0x120a4
	s_brev_b32 s52, 1
	v_lshlrev_b32_e32 v4, 2, v12
	v_mov_b32_e32 v5, 0
	v_add_u32_e32 v19, v16, v18
	s_movk_i32 s53, 0x4ff
	s_movk_i32 s54, 0xffcf
	s_mov_b32 s55, 0xc3e00000
	v_cmp_ne_u32_e64 s[6:7], 1, v6
	v_mov_b32_e32 v20, 0x43e00000
	s_branch .LBB0_1251

; DI void cvt_group(const Params& p, LAS unsigned char* lds, int group, int t_lo, int t_hi, int r, int I) {
;     ...
;     if (tid == 0) {
;         int t0 = 0, nj = 0;
;         if (group == 0) {
;             set_job(J, 0, p.in[11], (bf16_t*)(ws + WS_W0IN), DM, L0IN, DM, 0, 1, 0, 0, t0);
;             set_job(J, 1, p.in[13], (bf16_t*)(ws + WS_WUQ), 512, 1536, 512, 0, 1, 0, 0, t0);
;             set_job(J, 2, p.in[15], (bf16_t*)(ws + WS_WUKV), 256, 2048, 256, 0, 1, 0, 0, t0);
;             set_job(J, 3, p.in[23], (bf16_t*)(ws + WS_W0OUT), DM, DM, DM, 0, 1, 0, 0, t0);
;             set_job(J, 4, p.in[31], (bf16_t*)(ws + WS_W1IN), DM, L1IN, DM, 1, 1, 0, 0, t0); if (FP8_IN1) J[4].f8scale = 64.f;
;             set_job(J, 5, p.in[34], (bf16_t*)(ws + WS_W1OUT), DM, DM, DM, 0, 1, 0, 0, t0); if (FP8_OUT1) J[5].f8scale = 64.f;
;             set_job(J, 6, p.in[18], (bf16_t*)(ws + WS_GW), 128, 128, 128, 0, 16, 128 * 128, 128 * 128, t0);
;             set_job(J, 7, p.in[20], (bf16_t*)(ws + WS_GW + (size_t)16 * 128 * 128 * 2), 128, 128, 128, 0, 16, 128 * 128, 128 * 128, t0);
;             nj = 8;
;         } else if (group == 1) {
;             set_job(J, 0, p.in[24], (bf16_t*)(ws + WS_EG), DM, EFF, DM, 0, NEXP, (size_t)DM * EFF, (size_t)EFF * DM, t0);
;             set_job(J, 1, p.in[25], (bf16_t*)(ws + WS_EU), DM, EFF, DM, 0, NEXP, (size_t)DM * EFF, (size_t)EFF * DM, t0);
;             set_job(J, 2, p.in[26], (bf16_t*)(ws + WS_ED), EFF, DM, EFF, 0, NEXP, (size_t)DM * EFF, (size_t)EFF * DM, t0);
;             if (FP8_L0) { J[0].f8scale = 64.f; J[1].f8scale = 64.f; J[2].f8scale = 32.f; }
;             nj = 3;
;         } else {
;             set_job(J, 0, p.in[35], (bf16_t*)(ws + WS_EG + EXPW), DM, EFF, DM, 0, NEXP, (size_t)DM * EFF, (size_t)EFF * DM, t0); J[0].f8scale = 64.f;
;             set_job(J, 1, p.in[36], (bf16_t*)(ws + WS_EU + EXPW), DM, EFF, DM, 0, NEXP, (size_t)DM * EFF, (size_t)EFF * DM, t0); J[1].f8scale = 64.f;
;             set_job(J, 2, p.in[37], (bf16_t*)(ws + WS_ED + EXPW), EFF, DM, EFF, 0, NEXP, (size_t)DM * EFF, (size_t)EFF * DM, t0); J[2].f8scale = 32.f;
;             nj = 3;
;         }
;         J[nj].tile0 = t0; J[15].tile0 = nj;
;     }
;     __syncthreads();
;     const int nj = J[15].tile0, total = J[nj].tile0;
;     const int hi = min(t_hi, total);
;     const int row = tid >> 6, c4 = (tid & 63) * 4;
;     for (int gt = t_lo + r; gt < hi; gt += I) {
.LBB0_1640:
	s_add_u32 s16, s50, 0xf10e000
	s_addc_u32 s17, s51, 0
	s_add_u32 s14, s50, 0x1710e000
	s_addc_u32 s15, s51, 0
	s_abs_i32 s0, s23
	v_cvt_f32_u32_e32 v3, s0
	s_sub_i32 s5, 0, s0
	s_abs_i32 s4, s9
	s_ashr_i32 s1, s9, 31
	v_rcp_iflag_f32_e32 v3, v3
	v_and_b32_e32 v11, 0xff, v0
	v_lshlrev_b32_e32 v4, 1, v0
	v_mul_u32_u24_e32 v2, 0x410, v198
	v_mul_f32_e32 v3, 0x4f7ffffe, v3
	v_cvt_u32_f32_e32 v3, v3
	v_and_b32_e32 v10, 0xfc, v199
	v_and_b32_e32 v4, 32, v4
	v_lshl_add_u32 v16, v11, 2, 0
	v_readfirstlane_b32 s6, v3
	s_mul_i32 s5, s5, s6
	s_mul_hi_u32 s5, s6, s5
	s_add_i32 s6, s6, s5
	s_mul_hi_u32 s5, s4, s6
	s_mul_i32 s5, s5, s0
	s_sub_i32 s4, s4, s5
	s_sub_i32 s5, s4, s0
	s_cmp_ge_u32 s4, s0
	s_cselect_b32 s4, s5, s4
	s_sub_i32 s5, s4, s0
	s_cmp_ge_u32 s4, s0
	s_cselect_b32 s0, s5, s4
	s_xor_b32 s0, s0, s1
	s_sub_i32 s4, s0, s1
	v_mul_u32_u24_e32 v14, 0x410, v222
	v_mul_u32_u24_e32 v13, 0x410, v223
	v_cmp_eq_u32_e64 s[2:3], 0, v0
	v_mov_b32_e32 v199, 0
	v_lshl_add_u32 v15, v10, 2, 0
	v_and_or_b32 v1, v1, 16, v4
	s_cmp_lg_u32 s4, 0
	v_add_u32_e32 v12, v16, v2
	s_cbranch_scc0 .LBB0_1663
	s_waitcnt vmcnt(0)
	s_barrier
	s_and_saveexec_b64 s[0:1], s[2:3]
	s_cbranch_execz .LBB0_1644
	s_movk_i32 s8, 0x800
	s_mov_b32 s11, 0
	s_add_i32 s5, 0, 0x12000
	s_mov_b32 s10, s8
	v_mov_b32_e32 v2, s42
	v_mov_b32_e32 v3, s43
	v_mov_b32_e32 v4, s52
	v_mov_b32_e32 v5, s53
	v_mov_b32_e32 v6, s5
	s_movk_i32 s9, 0x200
	s_add_i32 s5, 0, 0x12010
	v_mov_b64_e32 v[24:25], s[10:11]
	ds_write_b128 v6, v[2:5]
	v_mov_b32_e32 v2, s5
	v_mov_b64_e32 v[22:23], s[8:9]
	s_add_i32 s5, 0, 0x12020
	s_mov_b32 s6, 0x100000
	ds_write_b128 v2, v[22:25]
	v_mov_b32_e32 v8, 64
	v_mov_b32_e32 v9, 0
	v_mov_b32_e32 v2, s5
	s_add_i32 s5, 0, 0x12028
	s_mov_b32 s7, s11
	s_mov_b32 s10, s6
	ds_write_b64 v2, v[8:9]
	v_mov_b32_e32 v2, s5
	v_mov_b64_e32 v[18:19], s[6:7]
	v_mov_b64_e32 v[20:21], s[10:11]
	s_add_i32 s5, 0, 0x12040
	ds_write2_b64 v2, v[18:19], v[20:21] offset1:1
	v_mov_b32_e32 v2, s44
	v_mov_b32_e32 v3, s45
	v_mov_b32_e32 v4, s16
	v_mov_b32_e32 v5, s17
	v_mov_b32_e32 v6, s5
	s_add_i32 s5, 0, 0x12050
	ds_write_b128 v6, v[2:5]
	v_mov_b32_e32 v2, s5
	s_add_i32 s5, 0, 0x12060
	ds_write_b128 v2, v[22:25]
	v_mov_b32_e32 v3, 0x800
	v_mov_b32_e32 v2, v8
	v_mov_b32_e32 v4, s5
	s_add_i32 s5, 0, 0x12068
	ds_write_b64 v4, v[2:3]
	v_mov_b32_e32 v2, s5
	s_add_i32 s5, 0, 0x12080
	ds_write2_b64 v2, v[18:19], v[20:21] offset1:1
	v_mov_b32_e32 v4, s46
	v_mov_b32_e32 v5, s47
	v_mov_b32_e32 v6, s14
	v_mov_b32_e32 v7, s15
	v_mov_b32_e32 v2, s5
	ds_write_b128 v2, v[4:7]
	v_mov_b32_e32 v2, 0x200
	s_add_i32 s5, 0, 0x12090
	v_mov_b32_e32 v4, v2
	v_mov_b32_e32 v5, v9
	v_mov_b32_e32 v6, s5
	s_add_i32 s5, 0, 0x120a0
	ds_write_b128 v6, v[2:5]
	v_mov_b32_e32 v9, 0x1000
	v_mov_b32_e32 v2, s5
	s_add_i32 s5, 0, 0x120a8
	ds_write_b64 v2, v[8:9]
	v_mov_b32_e32 v2, s5
	s_add_i32 s5, 0, 0x12038
	ds_write2_b64 v2, v[18:19], v[20:21] offset1:1
	v_mov_b32_e32 v2, 0x42800000
	v_mov_b32_e32 v3, s5
	s_add_i32 s5, 0, 0x12078
	ds_write_b32 v3, v2
	v_mov_b32_e32 v3, s5
	s_add_i32 s5, 0, 0x120b8
	ds_write_b32 v3, v2
	v_mov_b32_e32 v2, 0x42000000
	v_mov_b32_e32 v3, s5
	s_add_i32 s5, 0, 0x120e4
	ds_write_b32 v3, v2
	v_mov_b32_e32 v2, 0x1800
	v_mov_b32_e32 v3, s5
	s_add_i32 s5, 0, 0x123e4
	ds_write_b32 v3, v2
	v_mov_b32_e32 v2, 3
	v_mov_b32_e32 v3, s5
	ds_write_b32 v3, v2
.LBB0_1644:
	s_or_b64 exec, exec, s[0:1]
	s_add_i32 s0, 0, 0x123e4
	v_mov_b32_e32 v2, s0
	s_waitcnt lgkmcnt(0)
	s_barrier
	ds_read_b32 v2, v2
	s_sub_i32 s26, s23, s4
	s_mul_i32 s0, s26, 6
	s_sub_i32 s0, 0x800, s0
	s_max_i32 s0, s0, 0
	s_lshr_b32 s0, s0, 8
	s_cmpk_lg_i32 s23, 0x100
	s_cselect_b32 s0, 0, s0
	s_mul_i32 s0, s0, s4
	s_sub_i32 s1, 0x1800, s0
	s_sub_i32 s18, s22, s4
	s_add_i32 s18, s18, 0x1000
	s_add_i32 s0, s1, s22
	s_cmp_lt_i32 s22, s4
	s_cselect_b32 s18, s0, s18
	s_cselect_b32 s26, s4, s26
	s_cselect_b32 s1, 0x1800, s1
	s_waitcnt lgkmcnt(0)
	v_lshlrev_b32_e32 v3, 6, v2
	v_add_u32_e32 v3, 0, v3
	v_add_u32_e32 v3, 0x12024, v3
	ds_read_b32 v3, v3
	v_readfirstlane_b32 s19, v2
	s_waitcnt lgkmcnt(0)
	v_min_i32_e32 v17, s1, v3
	v_cmp_ge_i32_e32 vcc, s18, v17
	s_cbranch_vccnz .LBB0_1662
	s_cmp_gt_i32 s19, 1
	s_cselect_b64 s[0:1], -1, 0
	s_add_i32 s4, s19, -1
	s_cmp_lg_u32 s19, 2
	v_cndmask_b32_e64 v2, 0, 1, s[0:1]
	s_cselect_b64 s[0:1], -1, 0
	s_and_b32 s27, s4, -2
	s_or_b32 s30, s4, 1
	s_cmp_lg_u32 s4, s27
	v_cndmask_b32_e64 v4, 0, 1, s[0:1]
	s_cselect_b64 s[8:9], -1, 0
	v_cmp_ne_u32_e64 s[4:5], 1, v2
	s_add_i32 s31, 0, 0x120a4
	s_brev_b32 s34, 1
	v_lshlrev_b32_e32 v2, 2, v10
	v_mov_b32_e32 v3, 0
	v_add_u32_e32 v18, v15, v14
	s_movk_i32 s35, 0x4ff
	s_movk_i32 s36, 0xffcf
	s_mov_b32 s37, 0xc3e00000
	v_cmp_ne_u32_e64 s[6:7], 1, v4
	v_mov_b32_e32 v19, 0x43e00000
	s_branch .LBB0_1648
